# baseline (speedup 1.0000x reference)
.LBB3_6:
	s_or_b64 exec, exec, s[24:25]
	s_or_b32 s24, s16, 8
	s_ashr_i32 s25, s24, 31
	s_lshl_b64 s[24:25], s[24:25], 16
	s_add_u32 s9, s6, s24
	s_addc_u32 s16, s7, s25
	s_add_u32 s24, s9, s17
	s_addc_u32 s25, s16, 0
	s_add_i32 s9, 0, 0x18000
	s_add_i32 s16, s9, s31
	v_mov_b32_e32 v3, v140
	s_mov_b32 m0, s16
	v_mov_b32_e32 v130, v140
	s_add_i32 s51, s43, 0x8000
	global_load_lds_dwordx4 v3, s[24:25] sc0
	s_add_i32 m0, s16, 0x2000
	v_lshl_add_u64 v[4:5], s[24:25], 0, v[130:131]
	v_lshl_add_u64 v[4:5], v[4:5], 0, s[18:19]
	v_mov_b32_e32 v130, v1
	global_load_lds_dwordx4 v[4:5], off sc0
	s_mov_b64 s[18:19], 0x80
	v_lshl_add_u64 v[4:5], s[14:15], 0, v[130:131]
	v_lshl_add_u64 v[4:5], v[4:5], 0, s[18:19]
	s_mov_b32 m0, s51
	v_mov_b32_e32 v130, v1
	global_load_lds_dwordx4 v[4:5], off
	s_add_i32 s52, s43, 0xa000
	v_lshl_add_u64 v[4:5], s[14:15], 0, v[130:131]
	s_mov_b64 s[14:15], 0x10080
	v_lshl_add_u64 v[4:5], v[4:5], 0, s[14:15]
	s_mov_b32 m0, s52
	s_add_i32 s14, 0, 0x1c000
	v_mov_b32_e32 v130, v140
	global_load_lds_dwordx4 v[4:5], off
	s_add_i32 s15, s14, s31
	s_mov_b32 m0, s15
	v_lshl_add_u64 v[4:5], s[24:25], 0, v[130:131]
	v_lshl_add_u64 v[4:5], v[4:5], 0, s[20:21]
	v_mov_b32_e32 v130, v140
	global_load_lds_dwordx4 v[4:5], off sc0
	s_add_i32 m0, s15, 0x2000
	v_lshl_add_u64 v[4:5], s[24:25], 0, v[130:131]
	v_lshl_add_u64 v[4:5], v[4:5], 0, s[22:23]
	global_load_lds_dwordx4 v[4:5], off sc0
	v_lshlrev_b32_e32 v4, 6, v0
	v_lshlrev_b32_e32 v6, 2, v0
	v_and_b32_e32 v3, 48, v0
	v_and_b32_e32 v5, 0x3c0, v4
	v_and_b32_e32 v6, 32, v6
	v_bitop3_b32 v3, v3, v6, v5 bitop3:0x36
	v_add_u32_e32 v7, s9, v3
	s_lshl_b32 s9, s28, 3
	s_add_i32 s26, s26, s9
	s_sub_i32 s9, s26, s30
	v_add_u32_e32 v8, s14, v3
	s_sub_i32 s9, s9, s29
	s_lshl_b32 s14, s27, 3
	s_add_i32 s15, 0, 0x10000
	s_sub_i32 s9, s9, s14
	v_add_u32_e32 v5, s15, v3
	s_add_i32 s15, 0, 0x14000
	s_lshl_b32 s14, s9, 8
	v_add_u32_e32 v6, s15, v3
	s_ashr_i32 s15, s14, 31
	s_lshl_b64 s[14:15], s[14:15], 10
	s_add_u32 s4, s4, s14
	s_addc_u32 s5, s5, s15
	s_add_u32 s4, s4, 0x30100
	s_addc_u32 s5, s5, 0
	s_add_u32 s9, s12, s17
	s_addc_u32 s12, s13, 0
	s_add_u32 s6, s6, s9
	s_waitcnt vmcnt(10)
	s_barrier
	s_waitcnt vmcnt(6)
	v_lshlrev_b32_e32 v2, 13, v2
	s_addc_u32 s7, s7, s12
	s_waitcnt lgkmcnt(0)
	s_lshl_b32 s56, s8, 2
	s_add_u32 s56, s2, s56
	s_addc_u32 s57, s3, 0
	v_and_b32_e32 v254, 63, v0
	v_lshlrev_b32_e32 v254, 4, v254
	s_mov_b32 m0, 0x20000
	s_nop 0
	global_load_lds_dwordx4 v254, s[56:57]
	v_and_b32_e32 v4, 0x3000, v4
	v_add_u32_e32 v3, 0, v3
	v_or_b32_e32 v9, 0x800, v2
	v_or_b32_e32 v10, 0x1000, v2
	v_or_b32_e32 v11, 0x1800, v2
	s_add_u32 s6, s6, 0x180c00
	s_mov_b32 s12, 0xfffeff80
	s_movk_i32 s14, 0xff80
	s_mov_b32 s16, 0xfff7f400
	s_mov_b32 s18, 0xfff7f800
	s_mov_b32 s20, 0xfffd0000
	s_mov_b32 s22, 0xfffe0000
	s_mov_b32 s24, 0xfff7fc00
	s_mov_b32 s26, 0xfff80000
	s_mov_b32 s28, 0xffff0000
	s_movk_i32 s30, 0xf400
	s_movk_i32 s34, 0xf800
	s_mov_b32 s36, 0xfffd0080
	s_mov_b32 s38, 0xfffe0080
	s_movk_i32 s40, 0xfc00
	s_addc_u32 s7, s7, 0
	s_mov_b32 s53, -2
	v_add_u32_e32 v132, v5, v4
	v_add_u32_e32 v133, v3, v2
	v_add_u32_e32 v134, v3, v9
	v_add_u32_e32 v135, v3, v10
	v_add_u32_e32 v136, v3, v11
	s_mov_b32 s13, -1
	s_add_i32 s9, s43, 0xc000
	s_mov_b32 s15, -1
	s_add_i32 s42, s43, 0xe000
	v_add_u32_e32 v137, v6, v4
	s_mov_b32 s17, -1
	s_mov_b32 s19, -1
	s_mov_b32 s21, -1
	s_mov_b32 s23, -1
	s_mov_b32 s25, -1
	s_mov_b32 s27, -1
	v_add_u32_e32 v138, v7, v4
	s_mov_b32 s29, -1
	v_add_u32_e32 v139, v8, v4
	s_mov_b32 s31, -1
	s_mov_b32 s35, -1
	s_add_i32 s54, s43, 0x1a000
	s_mov_b32 s37, -1
	s_mov_b32 s39, -1
	s_mov_b32 s41, -1
	s_add_i32 s55, s43, 0x1e000
	v_mov_b32_e32 v2, v131
	v_mov_b32_e32 v3, v131
	v_mov_b32_e32 v4, v131
	v_mov_b32_e32 v5, v131
	v_mov_b32_e32 v10, v131
	v_mov_b32_e32 v11, v131
	v_mov_b32_e32 v12, v131
	v_mov_b32_e32 v13, v131
	v_mov_b32_e32 v6, v131
	v_mov_b32_e32 v7, v131
	v_mov_b32_e32 v8, v131
	v_mov_b32_e32 v9, v131
	v_mov_b32_e32 v14, v131
	v_mov_b32_e32 v15, v131
	v_mov_b32_e32 v16, v131
	v_mov_b32_e32 v17, v131
	v_mov_b32_e32 v30, v131
	v_mov_b32_e32 v31, v131
	v_mov_b32_e32 v32, v131
	v_mov_b32_e32 v33, v131
	v_mov_b32_e32 v42, v131
	v_mov_b32_e32 v43, v131
	v_mov_b32_e32 v44, v131
	v_mov_b32_e32 v45, v131
	v_mov_b32_e32 v38, v131
	v_mov_b32_e32 v39, v131
	v_mov_b32_e32 v40, v131
	v_mov_b32_e32 v41, v131
	v_mov_b32_e32 v46, v131
	v_mov_b32_e32 v47, v131
	v_mov_b32_e32 v48, v131
	v_mov_b32_e32 v49, v131
	v_mov_b32_e32 v18, v131
	v_mov_b32_e32 v19, v131
	v_mov_b32_e32 v20, v131
	v_mov_b32_e32 v21, v131
	v_mov_b32_e32 v26, v131
	v_mov_b32_e32 v27, v131
	v_mov_b32_e32 v28, v131
	v_mov_b32_e32 v29, v131
	v_mov_b32_e32 v22, v131
	v_mov_b32_e32 v23, v131
	v_mov_b32_e32 v24, v131
	v_mov_b32_e32 v25, v131
	v_mov_b32_e32 v34, v131
	v_mov_b32_e32 v35, v131
	v_mov_b32_e32 v36, v131
	v_mov_b32_e32 v37, v131
	v_mov_b32_e32 v50, v131
	v_mov_b32_e32 v51, v131
	v_mov_b32_e32 v52, v131
	v_mov_b32_e32 v53, v131
	v_mov_b32_e32 v58, v131
	v_mov_b32_e32 v59, v131
	v_mov_b32_e32 v60, v131
	v_mov_b32_e32 v61, v131
	v_mov_b32_e32 v54, v131
	v_mov_b32_e32 v55, v131
	v_mov_b32_e32 v56, v131
	v_mov_b32_e32 v57, v131
	v_mov_b32_e32 v62, v131
	v_mov_b32_e32 v63, v131
	v_mov_b32_e32 v64, v131
	v_mov_b32_e32 v65, v131
	v_mov_b32_e32 v66, v131
	v_mov_b32_e32 v67, v131
	v_mov_b32_e32 v68, v131
	v_mov_b32_e32 v69, v131
	v_mov_b32_e32 v74, v131
	v_mov_b32_e32 v75, v131
	v_mov_b32_e32 v76, v131
	v_mov_b32_e32 v77, v131
	v_mov_b32_e32 v70, v131
	v_mov_b32_e32 v71, v131
	v_mov_b32_e32 v72, v131
	v_mov_b32_e32 v73, v131
	v_mov_b32_e32 v78, v131
	v_mov_b32_e32 v79, v131
	v_mov_b32_e32 v80, v131
	v_mov_b32_e32 v81, v131
	v_mov_b32_e32 v98, v131
	v_mov_b32_e32 v99, v131
	v_mov_b32_e32 v100, v131
	v_mov_b32_e32 v101, v131
	v_mov_b32_e32 v106, v131
	v_mov_b32_e32 v107, v131
	v_mov_b32_e32 v108, v131
	v_mov_b32_e32 v109, v131
	v_mov_b32_e32 v102, v131
	v_mov_b32_e32 v103, v131
	v_mov_b32_e32 v104, v131
	v_mov_b32_e32 v105, v131
	v_mov_b32_e32 v110, v131
	v_mov_b32_e32 v111, v131
	v_mov_b32_e32 v112, v131
	v_mov_b32_e32 v113, v131
	v_mov_b32_e32 v82, v131
	v_mov_b32_e32 v83, v131
	v_mov_b32_e32 v84, v131
	v_mov_b32_e32 v85, v131
	v_mov_b32_e32 v90, v131
	v_mov_b32_e32 v91, v131
	v_mov_b32_e32 v92, v131
	v_mov_b32_e32 v93, v131
	v_mov_b32_e32 v86, v131
	v_mov_b32_e32 v87, v131
	v_mov_b32_e32 v88, v131
	v_mov_b32_e32 v89, v131
	v_mov_b32_e32 v94, v131
	v_mov_b32_e32 v95, v131
	v_mov_b32_e32 v96, v131
	v_mov_b32_e32 v97, v131
	v_mov_b32_e32 v114, v131
	v_mov_b32_e32 v115, v131
	v_mov_b32_e32 v116, v131
	v_mov_b32_e32 v117, v131
	v_mov_b32_e32 v118, v131
	v_mov_b32_e32 v119, v131
	v_mov_b32_e32 v120, v131
	v_mov_b32_e32 v121, v131
	v_mov_b32_e32 v122, v131
	v_mov_b32_e32 v123, v131
	v_mov_b32_e32 v124, v131
	v_mov_b32_e32 v125, v131
	v_mov_b32_e32 v126, v131
	v_mov_b32_e32 v127, v131
	v_mov_b32_e32 v128, v131
	v_mov_b32_e32 v129, v131
	s_barrier
